# mega stack + dense FFN up-projection row-panel group size 2 -> 4
# speedup vs baseline: 1.0178x; 1.0002x over previous
;     __device__ __forceinline__ size_t boff(const Unit& u) const { return (size_t)__builtin_amdgcn_readfirstlane(panel_e[u.pm]) * estride; }
; #define PG8_SETA(v, u) do { if constexpr (Sched::GATHER) { _Pragma("unroll") for (int h_ = 0; h_ < 2; ++h_) _Pragma("unroll") for (int i_ = 0; i_ < 2; ++i_) { \
;         int R_, C_; stage_rc(tid * 16 + i_ * 8192, R_, C_); int tok_ = S.arow[(u).pm * BM + h_ * HALF + R_]; tok_ = tok_ < 0 ? 0 : tok_; (v)[h_][i_] = (unsigned)(tok_ * K + C_) * 2u; } } } while (0)
; #define PG8_STAGE_A(bufoff, h, ptr, nsel) do { if constexpr (Sched::GATHER) { if (nsel) PG8_STAGE_X(bufoff, ptr, vAn[h], PG8_A_AUX); else PG8_STAGE_X(bufoff, ptr, vAc[h], PG8_A_AUX); } \
;         else PG8_STAGE_X(bufoff, (ptr) + (h) * hstep, voffA, PG8_A_AUX); } while (0)
; #define PG8_STAGE(bufoff, gbase, voff) PG8_STAGE_X(bufoff, gbase, voff, PG8_B_AUX)
; #define PG8_WAIT_V(n) asm volatile("s_waitcnt vmcnt(" #n ")" ::: "memory")
;     __host__ __device__ bool next(int i, Unit& u) const {
;         const long L = (long)i * G + c; if (L >= nwg) return false;
;         int wgid = (int)L; { const int q = nwg / NXCD, r = nwg % NXCD, xcd = wgid % NXCD; int off = wgid / NXCD; if (rev & 2) off = (xcd < r ? q + 1 : q) - 1 - off;
;             wgid = (xcd < r ? xcd * (q + 1) : r * (q + 1) + (xcd - r) * q) + off; }
;         const int nig = wgm * nN, gid = wgid / nig, fm = gid * wgm, gsz = (nM - fm) < wgm ? (nM - fm) : wgm;
;         u.pm = fm + ((wgid % nig) % gsz); u.pn = (wgid % nig) / gsz; if (rev & 1) u.pn = nN - 1 - u.pn; return true;
;     }
; template <class Epi, class Sched, bool ALIGN_EPI = false, bool SP2 = false>
; __device__ __forceinline__ void gemm_phase(PG8_LAS unsigned char* lds, const Gemm g, const Sched& S, const Epi& E) {
;     ...
;     const char* cA = Sched::GATHER ? (const char*)g.A : (const char*)g.A + (size_t)cur.pm * tstep; PG8_SETA(vAc, cur); const char* cB = (const char*)g.Bt + S.boff(cur) + (size_t)cur.pn * tstep;
;     S.a_ready(cur);
;     if constexpr (SP2) {
;         PG8_STAGE(PG8_SB(0, 0), cB, voffB); PG8_STAGE(PG8_SB(0, 1), cB + hstep, voffB); PG8_STAGE_A(PG8_SA(0, 0), 0, cA, false); PG8_STAGE_A(PG8_SA(0, 1), 1, cA, false);
;         if (wr == 1) PG8_BAR;
;         PG8_WAIT_V(2); PG8_BAR;
;         PG8_STAGE(PG8_SB(1, 0), cB + kstep, voffB); PG8_STAGE_A(PG8_SA(1, 0), 0, cA + kstep, false); PG8_STAGE(PG8_SB(1, 1), cB + hstep + kstep, voffB);
.LBB13_1397:
	v_cndmask_b32_e64 v1, 0, 1, s[38:39]
	s_andn2_b64 vcc, exec, s[4:5]
	v_cmp_ne_u32_e64 s[42:43], 1, v1
	s_cbranch_vccnz .LBB13_1513
	v_readlane_b32 s2, v249, 1
	v_readlane_b32 s3, v249, 2
	s_load_dwordx2 s[2:3], s[2:3], 0xe8
	s_mov_b32 s0, s77
	v_mov_b32_e32 v1, v0
	s_mov_b64 s[8:9], 0
	s_waitcnt lgkmcnt(0)
	s_add_u32 s10, s2, s8
	s_addc_u32 s11, s3, s9
	s_add_i32 s2, s0, 0
	s_add_u32 s14, s10, 0x20700000
	s_addc_u32 s15, s11, 0
	s_lshr_b32 s38, s68, 1
	s_mov_b32 s44, s56
	v_readlane_b32 s45, v249, 0
	s_add_u32 s16, s10, 0x22800000
	s_addc_u32 s17, s11, 0
	s_ashr_i32 s46, s45, 31
	s_lshr_b32 s0, s46, 29
	s_add_i32 s0, s45, s0
	s_ashr_i32 s39, s0, 3
	s_and_b32 s0, s0, -8
	s_sub_i32 s40, s45, s0
	s_add_i32 s47, s2, 0x10000
	s_add_i32 s50, s2, 0x14000
	s_add_i32 s51, s2, 0x18000
	s_add_i32 s56, s2, 0x1c000
	s_ashr_i32 s57, s44, 31
	s_and_b64 vcc, exec, s[42:43]
	s_mov_b64 s[6:7], -1
	s_cbranch_vccnz .LBB13_1420
	v_readlane_b32 s0, v249, 59
	v_readlane_b32 s1, v249, 60
	s_and_b64 s[0:1], s[0:1], exec
	s_cselect_b32 s3, 64, 0x42
	s_mul_i32 s76, s3, 22
	s_waitcnt vmcnt(0)
	v_mov_b32_e32 v8, v0
	s_cmp_ge_i32 s45, s76
	s_nop 0
	v_readfirstlane_b32 s6, v8
	s_cbranch_scc1 .LBB13_1419
	v_lshlrev_b32_e32 v1, 4, v8
	v_add_u32_e32 v3, 0x2000, v1
	v_ashrrev_i32_e32 v2, 31, v3
	v_lshrrev_b32_e32 v2, 22, v2
	v_add_u32_e32 v2, v3, v2
	v_ashrrev_i32_e32 v2, 10, v2
	v_mul_i32_i24_e32 v4, 0x400, v2
	v_sub_u32_e32 v3, v3, v4
	v_lshrrev_b32_e32 v4, 4, v3
	v_bitop3_b32 v4, v4, v3, 32 bitop3:0x6c
	v_ashrrev_i32_e32 v3, 31, v4
	v_lshrrev_b32_e32 v3, 26, v3
	v_add_u32_e32 v5, v4, v3
	v_lshlrev_b32_e32 v6, 3, v2
	v_ashrrev_i32_e32 v3, 6, v5
	v_and_b32_e32 v6, -16, v6
	v_add_u32_e32 v6, v3, v6
	v_and_b32_e32 v7, 3, v3
	s_mov_b32 s4, 0x1fffe0
	v_lshrrev_b32_e32 v9, 2, v6
	v_lshlrev_b32_e32 v10, 1, v6
	v_and_b32_e32 v5, 0xc0, v5
	v_and_or_b32 v7, v6, s4, v7
	v_and_b32_e32 v9, 4, v9
	v_and_b32_e32 v10, 24, v10
	v_sub_u32_e32 v4, v4, v5
	v_or3_b32 v7, v7, v9, v10
	v_lshlrev_b32_e32 v9, 5, v2
	v_ashrrev_i16_sdwa v4, v238, sext(v4) dst_sel:DWORD dst_unused:UNUSED_PAD src0_sel:DWORD src1_sel:BYTE_0
	v_and_b32_e32 v9, 32, v9
	v_bfe_i32 v4, v4, 0, 16
	s_ashr_i32 s12, s6, 6
	v_add_lshl_u32 v5, v9, v4, 1
	s_ashr_i32 s13, s6, 8
	s_lshl_b32 s7, s12, 10
	s_mul_i32 s0, s38, 0x1080000
	v_lshl_add_u32 v132, v7, 11, v5
	v_lshl_add_u32 v134, v6, 11, v5
	v_bfe_i32 v5, v8, 27, 1
	s_add_u32 s0, s10, s0
	v_lshrrev_b32_e32 v5, 22, v5
	s_addc_u32 s1, s11, 0
	v_add_u32_e32 v5, v1, v5
	v_writelane_b32 v249, s42, 55
	s_add_u32 s41, s0, 0x5400000
	v_and_b32_e32 v5, 0xfffffc00, v5
	v_writelane_b32 v249, s43, 56
	s_addc_u32 s42, s1, 0
	s_lshr_b32 s43, s76, 3
	s_and_b32 s48, s76, 4
	v_sub_u32_e32 v1, v1, v5
	s_add_i32 s49, s43, 1
	s_sub_i32 s0, s40, s48
	v_lshrrev_b32_e32 v5, 4, v1
	v_ashrrev_i32_e32 v6, 31, v8
	s_mul_i32 s53, s49, s48
	s_mul_i32 s0, s0, s43
	v_bitop3_b32 v1, v5, v1, 32 bitop3:0x6c
	v_lshrrev_b32_e32 v6, 26, v6
	s_add_i32 s0, s0, s53
	v_ashrrev_i32_e32 v5, 31, v1
	v_add_u32_e32 v6, v8, v6
	s_cmp_lt_i32 s40, s48
	s_mul_i32 s1, s40, s49
	v_lshrrev_b32_e32 v5, 26, v5
	v_ashrrev_i32_e32 v6, 6, v6
	v_add_u32_e32 v7, v1, v5
	v_lshlrev_b32_e32 v9, 3, v6
	s_cselect_b32 s0, s1, s0
	v_ashrrev_i32_e32 v5, 6, v7
	v_and_b32_e32 v9, -16, v9
	s_add_i32 s0, s0, s39
	v_add_u32_e32 v9, v5, v9
	v_and_b32_e32 v10, 3, v5
	s_mul_hi_i32 s1, s0, 0x2e8ba2e9
	v_and_or_b32 v10, v9, s4, v10
	s_lshr_b32 s4, s1, 31
	s_ashr_i32 s1, s1, 4
	s_add_i32 s1, s1, s4
	s_lshl_b32 s4, s1, 2
	v_and_b32_e32 v7, 0xc0, v7
	s_sub_i32 s5, s3, s4
	v_sub_u32_e32 v1, v1, v7
	s_min_i32 s5, s5, 4
	v_ashrrev_i16_sdwa v1, v238, sext(v1) dst_sel:DWORD dst_unused:UNUSED_PAD src0_sel:DWORD src1_sel:BYTE_0
	s_abs_i32 s18, s5
	v_bfe_i32 v7, v1, 0, 16
	v_cvt_f32_u32_e32 v1, s18
	s_sub_i32 s20, 0, s18
	s_mul_i32 s1, s1, 88
	s_sub_i32 s0, s0, s1
	v_rcp_iflag_f32_e32 v1, v1
	s_abs_i32 s19, s0
	s_xor_b32 s1, s0, s5
	s_ashr_i32 s1, s1, 31
	v_mul_f32_e32 v1, 0x4f7ffffe, v1
	v_cvt_u32_f32_e32 v1, v1
	v_lshrrev_b32_e32 v11, 2, v9
	v_lshlrev_b32_e32 v12, 1, v9
	v_and_b32_e32 v11, 4, v11
	v_readfirstlane_b32 s21, v1
	s_mul_i32 s20, s20, s21
	s_mul_hi_u32 s20, s21, s20
	s_add_i32 s21, s21, s20
	s_mul_hi_u32 s20, s19, s21
	s_mul_i32 s21, s20, s18
	s_sub_i32 s19, s19, s21
	s_add_i32 s21, s20, 1
	s_sub_i32 s22, s19, s18
	s_cmp_ge_u32 s19, s18
	s_cselect_b32 s20, s21, s20
	s_cselect_b32 s19, s22, s19
	s_add_i32 s21, s20, 1
	s_cmp_ge_u32 s19, s18
	s_cselect_b32 s18, s21, s20
	s_xor_b32 s18, s18, s1
	s_sub_i32 s26, s18, s1
	s_mul_i32 s1, s26, s5
	s_sub_i32 s0, s0, s1
	s_add_i32 s28, s4, s0
	s_ashr_i32 s29, s28, 31
	s_lshl_b64 s[0:1], s[28:29], 19
	s_add_u32 s30, s14, s0
	s_addc_u32 s31, s15, s1
	s_ashr_i32 s27, s26, 31
	v_and_b32_e32 v12, 24, v12
	s_lshl_b64 s[0:1], s[26:27], 19
	v_or3_b32 v10, v10, v11, v12
	v_lshlrev_b32_e32 v11, 5, v6
	s_add_u32 s34, s41, s0
	v_and_b32_e32 v11, 32, v11
	s_addc_u32 s35, s42, s1
	s_add_i32 s4, s47, s7
	v_add_lshl_u32 v11, v11, v7, 1
	s_add_i32 s5, s4, 0x2000
	v_lshl_add_u32 v136, v10, 11, v11
	s_mov_b32 m0, s4
	s_add_u32 s0, s34, 0x40000
	global_load_lds_dwordx4 v136, s[34:35]
	s_mov_b32 m0, s5
	s_addc_u32 s1, s35, 0
	s_add_i32 s29, s50, s7
	global_load_lds_dwordx4 v132, s[34:35]
	s_mov_b32 m0, s29
	s_add_i32 s52, s29, 0x2000
	s_add_i32 s58, s2, s7
	global_load_lds_dwordx4 v136, s[0:1]
	s_mov_b32 m0, s52
	s_add_i32 s59, s58, 0x2000
	v_lshl_add_u32 v138, v9, 11, v11
	global_load_lds_dwordx4 v132, s[0:1]
	s_mov_b32 m0, s58
	s_add_u32 s0, s30, 0x40000
	global_load_lds_dwordx4 v138, s[30:31]
	s_mov_b32 m0, s59
	s_addc_u32 s1, s31, 0
	s_add_i32 s60, s58, 0x4000
	global_load_lds_dwordx4 v134, s[30:31]
	s_mov_b32 m0, s60
	s_add_i32 s61, s58, 0x6000
	global_load_lds_dwordx4 v138, s[0:1]
	s_mov_b32 m0, s61
	s_cmp_eq_u32 s13, 1
	global_load_lds_dwordx4 v134, s[0:1]
	s_cselect_b64 s[0:1], -1, 0
	s_cmp_lg_u32 s13, 1
	s_cbranch_scc1 .LBB13_1402
